# v83 + prologue x to bf16 copy: four row pieces per lane in flight per trip instead of one
# baseline (speedup 1.0000x reference)
; __device__ __forceinline__ unsigned pk2(float lo, float hi) { return (unsigned)f2bf(lo) | ((unsigned)f2bf(hi) << 16); }
; __device__ __forceinline__ void ph_prologue(const Args& a, LAS unsigned char* lds) {
;     ...
;         const float* x = a.in[0]; bf16_t* XA = (bf16_t*)(a.ws + WS_XA);
;         for (size_t i = gt; i < (size_t)M * D / 8; i += ngt) { const f32x4 v0 = *(const f32x4*)(x + i * 8), v1 = *(const f32x4*)(x + i * 8 + 4);
;             u32x4 o; o.x = pk2(v0[0], v0[1]); o.y = pk2(v0[2], v0[3]); o.z = pk2(v1[0], v1[1]); o.w = pk2(v1[2], v1[3]); *(u32x4*)(XA + i * 8) = o; }
.LBB0_87:
	s_or_b64 exec, exec, s[4:5]
	s_mov_b32 s4, 0x400000
	v_cmp_gt_u32_e32 vcc, s4, v8
	s_and_saveexec_b64 s[4:5], vcc
	s_cbranch_execz .LBB0_90
	s_load_dwordx2 s[6:7], s[82:83], 0x0
	v_mov_b32_e32 v9, 0
	v_lshlrev_b64 v[4:5], 5, v[8:9]
	s_waitcnt lgkmcnt(0)
	v_lshl_add_u64 v[10:11], v[8:9], 4, s[0:1]
	v_lshlrev_b64 v[2:3], 5, v[6:7]
	v_lshl_add_u64 v[4:5], s[6:7], 0, v[4:5]
	s_mov_b64 s[6:7], 0x4100000
	v_lshl_add_u64 v[4:5], v[4:5], 0, 16
	v_lshl_add_u64 v[10:11], v[10:11], 0, s[6:7]
	v_lshlrev_b64 v[12:13], 4, v[6:7]
	s_mov_b64 s[6:7], 0
	s_movk_i32 s10, 0x7fff
	s_mov_b32 s11, 0xffff0000
	s_mov_b64 s[8:9], 0x3fffff
	v_mov_b64_e32 v[14:15], v[8:9]
	s_cmp_lg_u32 s22, 0x100
	s_cbranch_scc1 .LBB0_89
	s_mov_b32 s12, 8
.Lxa_loop:
	global_load_dwordx4 v[72:75], v[4:5], off offset:-16
	global_load_dwordx4 v[76:79], v[4:5], off
	v_lshl_add_u64 v[116:117], v[4:5], 0, v[2:3]
	global_load_dwordx4 v[80:83], v[116:117], off offset:-16
	global_load_dwordx4 v[84:87], v[116:117], off
	v_lshl_add_u64 v[118:119], v[116:117], 0, v[2:3]
	global_load_dwordx4 v[88:91], v[118:119], off offset:-16
	global_load_dwordx4 v[92:95], v[118:119], off
	v_lshl_add_u64 v[120:121], v[118:119], 0, v[2:3]
	global_load_dwordx4 v[96:99], v[120:121], off offset:-16
	global_load_dwordx4 v[100:103], v[120:121], off
	v_lshl_add_u64 v[4:5], v[120:121], 0, v[2:3]
	v_lshl_add_u64 v[122:123], v[10:11], 0, v[12:13]
	v_lshl_add_u64 v[68:69], v[122:123], 0, v[12:13]
	v_lshl_add_u64 v[70:71], v[68:69], 0, v[12:13]
	s_waitcnt vmcnt(6)
	v_bfe_u32 v104, v72, 16, 1
	v_bfe_u32 v105, v73, 16, 1
	v_bfe_u32 v106, v74, 16, 1
	v_bfe_u32 v107, v75, 16, 1
	v_bfe_u32 v108, v76, 16, 1
	v_bfe_u32 v109, v77, 16, 1
	v_bfe_u32 v110, v78, 16, 1
	v_bfe_u32 v111, v79, 16, 1
	v_add3_u32 v104, v72, v104, s10
	v_add3_u32 v105, v73, v105, s10
	v_add3_u32 v106, v74, v106, s10
	v_add3_u32 v107, v75, v107, s10
	v_add3_u32 v108, v76, v108, s10
	v_add3_u32 v109, v77, v109, s10
	v_add3_u32 v110, v78, v110, s10
	v_add3_u32 v111, v79, v111, s10
	v_lshrrev_b32_e32 v104, 16, v104
	v_lshrrev_b32_e32 v106, 16, v106
	v_lshrrev_b32_e32 v108, 16, v108
	v_lshrrev_b32_e32 v110, 16, v110
	v_and_or_b32 v112, v105, s11, v104
	v_and_or_b32 v113, v107, s11, v106
	v_and_or_b32 v114, v109, s11, v108
	v_and_or_b32 v115, v111, s11, v110
	global_store_dwordx4 v[10:11], v[112:115], off
	s_nop 1
	s_waitcnt vmcnt(5)
	v_bfe_u32 v104, v80, 16, 1
	v_bfe_u32 v105, v81, 16, 1
	v_bfe_u32 v106, v82, 16, 1
	v_bfe_u32 v107, v83, 16, 1
	v_bfe_u32 v108, v84, 16, 1
	v_bfe_u32 v109, v85, 16, 1
	v_bfe_u32 v110, v86, 16, 1
	v_bfe_u32 v111, v87, 16, 1
	v_add3_u32 v104, v80, v104, s10
	v_add3_u32 v105, v81, v105, s10
	v_add3_u32 v106, v82, v106, s10
	v_add3_u32 v107, v83, v107, s10
	v_add3_u32 v108, v84, v108, s10
	v_add3_u32 v109, v85, v109, s10
	v_add3_u32 v110, v86, v110, s10
	v_add3_u32 v111, v87, v111, s10
	v_lshrrev_b32_e32 v104, 16, v104
	v_lshrrev_b32_e32 v106, 16, v106
	v_lshrrev_b32_e32 v108, 16, v108
	v_lshrrev_b32_e32 v110, 16, v110
	v_and_or_b32 v112, v105, s11, v104
	v_and_or_b32 v113, v107, s11, v106
	v_and_or_b32 v114, v109, s11, v108
	v_and_or_b32 v115, v111, s11, v110
	global_store_dwordx4 v[122:123], v[112:115], off
	s_nop 1
	s_waitcnt vmcnt(4)
	v_bfe_u32 v104, v88, 16, 1
	v_bfe_u32 v105, v89, 16, 1
	v_bfe_u32 v106, v90, 16, 1
	v_bfe_u32 v107, v91, 16, 1
	v_bfe_u32 v108, v92, 16, 1
	v_bfe_u32 v109, v93, 16, 1
	v_bfe_u32 v110, v94, 16, 1
	v_bfe_u32 v111, v95, 16, 1
	v_add3_u32 v104, v88, v104, s10
	v_add3_u32 v105, v89, v105, s10
	v_add3_u32 v106, v90, v106, s10
	v_add3_u32 v107, v91, v107, s10
	v_add3_u32 v108, v92, v108, s10
	v_add3_u32 v109, v93, v109, s10
	v_add3_u32 v110, v94, v110, s10
	v_add3_u32 v111, v95, v111, s10
	v_lshrrev_b32_e32 v104, 16, v104
	v_lshrrev_b32_e32 v106, 16, v106
	v_lshrrev_b32_e32 v108, 16, v108
	v_lshrrev_b32_e32 v110, 16, v110
	v_and_or_b32 v112, v105, s11, v104
	v_and_or_b32 v113, v107, s11, v106
	v_and_or_b32 v114, v109, s11, v108
	v_and_or_b32 v115, v111, s11, v110
	global_store_dwordx4 v[68:69], v[112:115], off
	s_nop 1
	s_waitcnt vmcnt(3)
	v_bfe_u32 v104, v96, 16, 1
	v_bfe_u32 v105, v97, 16, 1
	v_bfe_u32 v106, v98, 16, 1
	v_bfe_u32 v107, v99, 16, 1
	v_bfe_u32 v108, v100, 16, 1
	v_bfe_u32 v109, v101, 16, 1
	v_bfe_u32 v110, v102, 16, 1
	v_bfe_u32 v111, v103, 16, 1
	v_add3_u32 v104, v96, v104, s10
	v_add3_u32 v105, v97, v105, s10
	v_add3_u32 v106, v98, v106, s10
	v_add3_u32 v107, v99, v107, s10
	v_add3_u32 v108, v100, v108, s10
	v_add3_u32 v109, v101, v109, s10
	v_add3_u32 v110, v102, v110, s10
	v_add3_u32 v111, v103, v111, s10
	v_lshrrev_b32_e32 v104, 16, v104
	v_lshrrev_b32_e32 v106, 16, v106
	v_lshrrev_b32_e32 v108, 16, v108
	v_lshrrev_b32_e32 v110, 16, v110
	v_and_or_b32 v112, v105, s11, v104
	v_and_or_b32 v113, v107, s11, v106
	v_and_or_b32 v114, v109, s11, v108
	v_and_or_b32 v115, v111, s11, v110
	global_store_dwordx4 v[70:71], v[112:115], off
	v_lshl_add_u64 v[10:11], v[70:71], 0, v[12:13]
	s_sub_i32 s12, s12, 1
	s_cmp_lg_u32 s12, 0
	s_cbranch_scc1 .Lxa_loop
	s_branch .LBB0_90
